# v26: v25 with each wave's conversion-block loads issued one row iteration ahead (no cold-HBM load on the row's wait)
# baseline (speedup 1.0000x reference)
.Lx14_linit:
	s_barrier
	v_mbcnt_lo_u32_b32 v1, -1, 0
	v_mbcnt_hi_u32_b32 v1, -1, v1
	v_lshlrev_b32_e32 v2, 4, v1
	v_lshrrev_b32_e32 v3, 3, v1
	v_lshlrev_b32_e32 v3, 2, v3
	v_and_b32_e32 v4, 31, v1
	v_lshlrev_b32_e32 v4, 2, v4
	v_lshrrev_b32_e32 v9, 5, v1
	v_lshl_add_u32 v4, v9, 8, v4
	v_lshlrev_b32_e32 v9, 5, v1
	s_load_dwordx4 s[28:31], s[74:75], 0x100
	s_add_u32 s4, s54, 0x8c00000
	s_addc_u32 s5, s55, 0
	s_add_u32 s6, s54, 0x29400000
	s_addc_u32 s7, s55, 0
	s_add_u32 s8, s54, 0x21200000
	s_addc_u32 s9, s55, 0
	s_add_u32 s10, s54, 0x49c00000
	s_addc_u32 s11, s55, 0
	s_add_u32 s12, s54, 0x19000000
	s_addc_u32 s13, s55, 0
	s_add_u32 s14, s54, 0xc00000
	s_addc_u32 s15, s55, 0
	s_add_u32 s16, s54, 0x1000000
	s_addc_u32 s17, s55, 0
	s_add_u32 s20, s54, 0xc400
	s_addc_u32 s21, s55, 0
	s_mov_b32 s18, -1
	s_mov_b32 s19, 0
	s_add_i32 s25, s2, 0xffffff80
	s_lshl_b32 s25, s25, 3
	s_add_i32 s25, s25, s82
	s_and_b32 s40, s25, 15
	s_lshr_b32 s41, s25, 4
	s_lshl_b32 s42, s40, 18
	s_lshl_b32 s43, s41, 7
	s_add_i32 s42, s42, s43
	s_lshl_b32 s43, s41, 15
	s_lshl_b32 s40, s40, 6
	s_add_i32 s43, s43, s40
	s_load_dwordx2 s[44:45], s[74:75], 0x130
	v_lshrrev_b32_e32 v240, 1, v1
	v_and_b32_e32 v241, 1, v1
	v_lshlrev_b32_e32 v242, 13, v240
	v_lshl_add_u32 v242, v241, 6, v242
	v_lshlrev_b32_e32 v243, 10, v240
	v_lshl_add_u32 v243, v241, 5, v243
	v_mul_u32_u24_e32 v244, 0x84, v240
	v_lshl_add_u32 v244, v241, 6, v244
	v_mul_u32_u24_e32 v245, 0x840, v241
	v_lshl_add_u32 v245, v240, 2, v245
	s_mul_i32 s40, s82, 0x1100
	s_add_i32 s40, s40, 0x1000
	v_add_u32_e32 v244, s40, v244
	v_add_u32_e32 v245, s40, v245
	s_lshr_b32 s100, s25, 8
	s_and_b32 s25, s25, 0xff
	s_mov_b32 s24, 0
	s_mov_b32 s26, 0
	s_waitcnt lgkmcnt(0)
	s_add_u32 s44, s44, 0x8000000
	s_addc_u32 s45, s45, 0
	s_add_u32 s44, s44, s42
	s_addc_u32 s45, s45, 0
	s_add_u32 s46, s54, 0x1400000
	s_addc_u32 s47, s55, 0
	s_add_u32 s46, s46, s43
	s_addc_u32 s47, s47, 0
	global_load_dwordx4 v[200:203], v242, s[44:45] nt
	global_load_dwordx4 v[204:207], v242, s[44:45] offset:16 nt
	global_load_dwordx4 v[208:211], v242, s[44:45] offset:32 nt
	global_load_dwordx4 v[212:215], v242, s[44:45] offset:48 nt
	global_load_dwordx4 v[10:13], v9, s[28:29]
	global_load_dwordx4 v[14:17], v9, s[28:29] offset:16
	global_load_dwordx4 v[18:21], v9, s[28:29] offset:2048
	global_load_dwordx4 v[22:25], v9, s[28:29] offset:2064
	global_load_dwordx4 v[42:45], v9, s[30:31]
	global_load_dwordx4 v[46:49], v9, s[30:31] offset:16
	global_load_dwordx4 v[50:53], v9, s[30:31] offset:2048
	global_load_dwordx4 v[54:57], v9, s[30:31] offset:2064
	v_add_u32_e32 v9, 0x1000, v9
	global_load_dwordx4 v[26:29], v9, s[28:29]
	global_load_dwordx4 v[30:33], v9, s[28:29] offset:16
	global_load_dwordx4 v[34:37], v9, s[28:29] offset:2048
	global_load_dwordx4 v[38:41], v9, s[28:29] offset:2064
	global_load_dwordx4 v[58:61], v9, s[30:31]
	global_load_dwordx4 v[62:65], v9, s[30:31] offset:16
	global_load_dwordx4 v[66:69], v9, s[30:31] offset:2048
	global_load_dwordx4 v[70:73], v9, s[30:31] offset:2064
	s_waitcnt vmcnt(0)

.Lx14_ready:
	global_load_dwordx4 v[80:83], v5, s[4:5] sc1
	global_load_dwordx4 v[84:87], v5, s[4:5] offset:1024 sc1
	global_load_dwordx4 v[88:91], v5, s[4:5] offset:2048 sc1
	global_load_dwordx4 v[92:95], v5, s[4:5] offset:3072 sc1
	global_load_dwordx4 v[96:99], v5, s[6:7] sc1
	global_load_dwordx4 v[100:103], v5, s[6:7] offset:1024 sc1
	global_load_dwordx4 v[104:107], v5, s[6:7] offset:2048 sc1
	global_load_dwordx4 v[108:111], v5, s[6:7] offset:3072 sc1
	s_waitcnt vmcnt(0)
	ds_write2_b32 v244, v200, v201 offset0:0 offset1:1
	ds_write2_b32 v244, v202, v203 offset0:2 offset1:3
	ds_write2_b32 v244, v204, v205 offset0:4 offset1:5
	ds_write2_b32 v244, v206, v207 offset0:6 offset1:7
	ds_write2_b32 v244, v208, v209 offset0:8 offset1:9
	ds_write2_b32 v244, v210, v211 offset0:10 offset1:11
	ds_write2_b32 v244, v212, v213 offset0:12 offset1:13
	ds_write2_b32 v244, v214, v215 offset0:14 offset1:15
	ds_read_b32 v216, v245
	ds_read_b32 v217, v245 offset:132
	ds_read_b32 v218, v245 offset:264
	ds_read_b32 v219, v245 offset:396
	ds_read_b32 v220, v245 offset:528
	ds_read_b32 v221, v245 offset:660
	ds_read_b32 v222, v245 offset:792
	ds_read_b32 v223, v245 offset:924
	ds_read_b32 v224, v245 offset:1056
	ds_read_b32 v225, v245 offset:1188
	ds_read_b32 v226, v245 offset:1320
	ds_read_b32 v227, v245 offset:1452
	ds_read_b32 v228, v245 offset:1584
	ds_read_b32 v229, v245 offset:1716
	ds_read_b32 v230, v245 offset:1848
	ds_read_b32 v231, v245 offset:1980
	s_lshl_b32 s40, s24, 21
	s_cmp_ge_u32 s24, 25
	s_cselect_b32 s41, 0x1000000, 0
	s_add_i32 s40, s40, s41
	s_add_u32 s40, s46, s40
	s_addc_u32 s41, s47, 0
	s_waitcnt lgkmcnt(0)
	s_add_i32 s48, s24, 1
	s_min_u32 s48, s48, 31
	s_lshl_b32 s48, s48, 22
	s_add_u32 s48, s44, s48
	s_addc_u32 s49, s45, 0
	global_load_dwordx4 v[200:203], v242, s[48:49] nt
	global_load_dwordx4 v[204:207], v242, s[48:49] offset:16 nt
	global_load_dwordx4 v[208:211], v242, s[48:49] offset:32 nt
	global_load_dwordx4 v[212:215], v242, s[48:49] offset:48 nt
	v_cvt_pk_bf16_f32 v232, v216, v217
	v_cvt_pk_bf16_f32 v233, v218, v219
	v_cvt_pk_bf16_f32 v234, v220, v221
	v_cvt_pk_bf16_f32 v235, v222, v223
	v_cvt_pk_bf16_f32 v236, v224, v225
	v_cvt_pk_bf16_f32 v237, v226, v227
	v_cvt_pk_bf16_f32 v238, v228, v229
	v_cvt_pk_bf16_f32 v239, v230, v231
	global_store_dwordx4 v243, v[232:235], s[40:41] nt
	global_store_dwordx4 v243, v[236:239], s[40:41] offset:16 nt
	v_lshlrev_b32_e32 v168, 16, v80
	v_lshlrev_b32_e32 v169, 16, v96
	v_add_f32_e32 v160, v168, v169
	v_and_b32_e32 v168, 0xffff0000, v80
	v_and_b32_e32 v169, 0xffff0000, v96
	v_add_f32_e32 v161, v168, v169
	v_lshlrev_b32_e32 v168, 16, v81
	v_lshlrev_b32_e32 v169, 16, v97
	v_add_f32_e32 v162, v168, v169
	v_and_b32_e32 v168, 0xffff0000, v81
	v_and_b32_e32 v169, 0xffff0000, v97
	v_add_f32_e32 v163, v168, v169
	v_lshlrev_b32_e32 v168, 16, v82
	v_lshlrev_b32_e32 v169, 16, v98
	v_add_f32_e32 v164, v168, v169
	v_and_b32_e32 v168, 0xffff0000, v82
	v_and_b32_e32 v169, 0xffff0000, v98
	v_add_f32_e32 v165, v168, v169
	v_lshlrev_b32_e32 v168, 16, v83
	v_lshlrev_b32_e32 v169, 16, v99
	v_add_f32_e32 v166, v168, v169
	v_and_b32_e32 v168, 0xffff0000, v83
	v_and_b32_e32 v169, 0xffff0000, v99
	v_add_f32_e32 v167, v168, v169
	v_add_f32_e32 v170, v160, v161
	v_add_f32_e32 v170, v170, v162
	v_add_f32_e32 v170, v170, v163
	v_add_f32_e32 v170, v170, v164
	v_add_f32_e32 v170, v170, v165
	v_add_f32_e32 v170, v170, v166
	v_add_f32_e32 v170, v170, v167
	s_nop 1
	v_add_f32_dpp v170, v170, v170 quad_perm:[1,0,3,2] row_mask:0xf bank_mask:0xf bound_ctrl:1
	s_nop 1
	v_add_f32_dpp v170, v170, v170 quad_perm:[2,3,0,1] row_mask:0xf bank_mask:0xf bound_ctrl:1
	s_nop 1
	v_add_f32_dpp v170, v170, v170 row_half_mirror row_mask:0xf bank_mask:0xf bound_ctrl:1
	v_mul_f32_e32 v170, 0x3c800000, v170
	v_sub_f32_e32 v160, v160, v170
	v_sub_f32_e32 v161, v161, v170
	v_sub_f32_e32 v162, v162, v170
	v_sub_f32_e32 v163, v163, v170
	v_sub_f32_e32 v164, v164, v170
	v_sub_f32_e32 v165, v165, v170
	v_sub_f32_e32 v166, v166, v170
	v_sub_f32_e32 v167, v167, v170
	v_mul_f32_e32 v171, v160, v160
	v_fmac_f32_e32 v171, v161, v161
	v_fmac_f32_e32 v171, v162, v162
	v_fmac_f32_e32 v171, v163, v163
	v_fmac_f32_e32 v171, v164, v164
	v_fmac_f32_e32 v171, v165, v165
	v_fmac_f32_e32 v171, v166, v166
	v_fmac_f32_e32 v171, v167, v167
	s_nop 1
	v_add_f32_dpp v171, v171, v171 quad_perm:[1,0,3,2] row_mask:0xf bank_mask:0xf bound_ctrl:1
	s_nop 1
	v_add_f32_dpp v171, v171, v171 quad_perm:[2,3,0,1] row_mask:0xf bank_mask:0xf bound_ctrl:1
	s_nop 1
	v_add_f32_dpp v171, v171, v171 row_half_mirror row_mask:0xf bank_mask:0xf bound_ctrl:1
	v_mov_b32_e32 v172, 0x3a27c5ac
	v_fmac_f32_e32 v172, 0x3c800000, v171
	v_rsq_f32_e32 v172, v172
	v_add_f32_e32 v173, v144, v148
	s_nop 0
	v_mul_f32_e32 v160, v160, v172
	v_mul_f32_e32 v161, v161, v172
	v_mul_f32_e32 v162, v162, v172
	v_mul_f32_e32 v163, v163, v172
	v_mul_f32_e32 v164, v164, v172
	v_mul_f32_e32 v165, v165, v172
	v_mul_f32_e32 v166, v166, v172
	v_mul_f32_e32 v167, v167, v172
	v_fma_f32 v160, v10, v160, v42
	v_fma_f32 v161, v11, v161, v43
	v_fma_f32 v162, v12, v162, v44
	v_fma_f32 v163, v13, v163, v45
	v_fma_f32 v164, v14, v164, v46
	v_fma_f32 v165, v15, v165, v47
	v_fma_f32 v166, v16, v166, v48
	v_fma_f32 v167, v17, v167, v49
	v_lshlrev_b32_e32 v168, 16, v112
	v_fmac_f32_e32 v160, v173, v168
	v_and_b32_e32 v169, 0xffff0000, v112
	v_fmac_f32_e32 v161, v173, v169
	v_lshlrev_b32_e32 v168, 16, v128
	v_mul_f32_e32 v160, v160, v168
	v_and_b32_e32 v169, 0xffff0000, v128
	v_mul_f32_e32 v161, v161, v169
	v_lshlrev_b32_e32 v168, 16, v113
	v_fmac_f32_e32 v162, v173, v168
	v_and_b32_e32 v169, 0xffff0000, v113
	v_fmac_f32_e32 v163, v173, v169
	v_lshlrev_b32_e32 v168, 16, v129
	v_mul_f32_e32 v162, v162, v168
	v_and_b32_e32 v169, 0xffff0000, v129
	v_mul_f32_e32 v163, v163, v169
	v_lshlrev_b32_e32 v168, 16, v114
	v_fmac_f32_e32 v164, v173, v168
	v_and_b32_e32 v169, 0xffff0000, v114
	v_fmac_f32_e32 v165, v173, v169
	v_lshlrev_b32_e32 v168, 16, v130
	v_mul_f32_e32 v164, v164, v168
	v_and_b32_e32 v169, 0xffff0000, v130
	v_mul_f32_e32 v165, v165, v169
	v_lshlrev_b32_e32 v168, 16, v115
	v_fmac_f32_e32 v166, v173, v168
	v_and_b32_e32 v169, 0xffff0000, v115
	v_fmac_f32_e32 v167, v173, v169
	v_lshlrev_b32_e32 v168, 16, v131
	v_mul_f32_e32 v166, v166, v168
	v_and_b32_e32 v169, 0xffff0000, v131
	v_mul_f32_e32 v167, v167, v169
	v_cvt_pk_bf16_f32 v180, v160, v161
	v_cvt_pk_bf16_f32 v181, v162, v163
	v_cvt_pk_bf16_f32 v182, v164, v165
	v_cvt_pk_bf16_f32 v183, v166, v167
	global_store_dwordx4 v5, v[180:183], s[12:13]
	v_lshlrev_b32_e32 v168, 16, v84
	v_lshlrev_b32_e32 v169, 16, v100
	v_add_f32_e32 v160, v168, v169
	v_and_b32_e32 v168, 0xffff0000, v84
	v_and_b32_e32 v169, 0xffff0000, v100
	v_add_f32_e32 v161, v168, v169
	v_lshlrev_b32_e32 v168, 16, v85
	v_lshlrev_b32_e32 v169, 16, v101
	v_add_f32_e32 v162, v168, v169
	v_and_b32_e32 v168, 0xffff0000, v85
	v_and_b32_e32 v169, 0xffff0000, v101
	v_add_f32_e32 v163, v168, v169
	v_lshlrev_b32_e32 v168, 16, v86
	v_lshlrev_b32_e32 v169, 16, v102
	v_add_f32_e32 v164, v168, v169
	v_and_b32_e32 v168, 0xffff0000, v86
	v_and_b32_e32 v169, 0xffff0000, v102
	v_add_f32_e32 v165, v168, v169
	v_lshlrev_b32_e32 v168, 16, v87
	v_lshlrev_b32_e32 v169, 16, v103
	v_add_f32_e32 v166, v168, v169
	v_and_b32_e32 v168, 0xffff0000, v87
	v_and_b32_e32 v169, 0xffff0000, v103
	v_add_f32_e32 v167, v168, v169
	v_add_f32_e32 v170, v160, v161
	v_add_f32_e32 v170, v170, v162
	v_add_f32_e32 v170, v170, v163
	v_add_f32_e32 v170, v170, v164
	v_add_f32_e32 v170, v170, v165
	v_add_f32_e32 v170, v170, v166
	v_add_f32_e32 v170, v170, v167
	s_nop 1
	v_add_f32_dpp v170, v170, v170 quad_perm:[1,0,3,2] row_mask:0xf bank_mask:0xf bound_ctrl:1
	s_nop 1
	v_add_f32_dpp v170, v170, v170 quad_perm:[2,3,0,1] row_mask:0xf bank_mask:0xf bound_ctrl:1
	s_nop 1
	v_add_f32_dpp v170, v170, v170 row_half_mirror row_mask:0xf bank_mask:0xf bound_ctrl:1
	v_mul_f32_e32 v170, 0x3c800000, v170
	v_sub_f32_e32 v160, v160, v170
	v_sub_f32_e32 v161, v161, v170
	v_sub_f32_e32 v162, v162, v170
	v_sub_f32_e32 v163, v163, v170
	v_sub_f32_e32 v164, v164, v170
	v_sub_f32_e32 v165, v165, v170
	v_sub_f32_e32 v166, v166, v170
	v_sub_f32_e32 v167, v167, v170
	v_mul_f32_e32 v171, v160, v160
	v_fmac_f32_e32 v171, v161, v161
	v_fmac_f32_e32 v171, v162, v162
	v_fmac_f32_e32 v171, v163, v163
	v_fmac_f32_e32 v171, v164, v164
	v_fmac_f32_e32 v171, v165, v165
	v_fmac_f32_e32 v171, v166, v166
	v_fmac_f32_e32 v171, v167, v167
	s_nop 1
	v_add_f32_dpp v171, v171, v171 quad_perm:[1,0,3,2] row_mask:0xf bank_mask:0xf bound_ctrl:1
	s_nop 1
	v_add_f32_dpp v171, v171, v171 quad_perm:[2,3,0,1] row_mask:0xf bank_mask:0xf bound_ctrl:1
	s_nop 1
	v_add_f32_dpp v171, v171, v171 row_half_mirror row_mask:0xf bank_mask:0xf bound_ctrl:1
	v_mov_b32_e32 v172, 0x3a27c5ac
	v_fmac_f32_e32 v172, 0x3c800000, v171
	v_rsq_f32_e32 v172, v172
	v_add_f32_e32 v173, v145, v149
	s_nop 0
	v_mul_f32_e32 v160, v160, v172
	v_mul_f32_e32 v161, v161, v172
	v_mul_f32_e32 v162, v162, v172
	v_mul_f32_e32 v163, v163, v172
	v_mul_f32_e32 v164, v164, v172
	v_mul_f32_e32 v165, v165, v172
	v_mul_f32_e32 v166, v166, v172
	v_mul_f32_e32 v167, v167, v172
	v_fma_f32 v160, v18, v160, v50
	v_fma_f32 v161, v19, v161, v51
	v_fma_f32 v162, v20, v162, v52
	v_fma_f32 v163, v21, v163, v53
	v_fma_f32 v164, v22, v164, v54
	v_fma_f32 v165, v23, v165, v55
	v_fma_f32 v166, v24, v166, v56
	v_fma_f32 v167, v25, v167, v57
	v_lshlrev_b32_e32 v168, 16, v116
	v_fmac_f32_e32 v160, v173, v168
	v_and_b32_e32 v169, 0xffff0000, v116
	v_fmac_f32_e32 v161, v173, v169
	v_lshlrev_b32_e32 v168, 16, v132
	v_mul_f32_e32 v160, v160, v168
	v_and_b32_e32 v169, 0xffff0000, v132
	v_mul_f32_e32 v161, v161, v169
	v_lshlrev_b32_e32 v168, 16, v117
	v_fmac_f32_e32 v162, v173, v168
	v_and_b32_e32 v169, 0xffff0000, v117
	v_fmac_f32_e32 v163, v173, v169
	v_lshlrev_b32_e32 v168, 16, v133
	v_mul_f32_e32 v162, v162, v168
	v_and_b32_e32 v169, 0xffff0000, v133
	v_mul_f32_e32 v163, v163, v169
	v_lshlrev_b32_e32 v168, 16, v118
	v_fmac_f32_e32 v164, v173, v168
	v_and_b32_e32 v169, 0xffff0000, v118
	v_fmac_f32_e32 v165, v173, v169
	v_lshlrev_b32_e32 v168, 16, v134
	v_mul_f32_e32 v164, v164, v168
	v_and_b32_e32 v169, 0xffff0000, v134
	v_mul_f32_e32 v165, v165, v169
	v_lshlrev_b32_e32 v168, 16, v119
	v_fmac_f32_e32 v166, v173, v168
	v_and_b32_e32 v169, 0xffff0000, v119
	v_fmac_f32_e32 v167, v173, v169
	v_lshlrev_b32_e32 v168, 16, v135
	v_mul_f32_e32 v166, v166, v168
	v_and_b32_e32 v169, 0xffff0000, v135
	v_mul_f32_e32 v167, v167, v169
	v_cvt_pk_bf16_f32 v184, v160, v161
	v_cvt_pk_bf16_f32 v185, v162, v163
	v_cvt_pk_bf16_f32 v186, v164, v165
	v_cvt_pk_bf16_f32 v187, v166, v167
	global_store_dwordx4 v5, v[184:187], s[12:13] offset:1024
	v_lshlrev_b32_e32 v168, 16, v88
	v_lshlrev_b32_e32 v169, 16, v104
	v_add_f32_e32 v160, v168, v169
	v_and_b32_e32 v168, 0xffff0000, v88
	v_and_b32_e32 v169, 0xffff0000, v104
	v_add_f32_e32 v161, v168, v169
	v_lshlrev_b32_e32 v168, 16, v89
	v_lshlrev_b32_e32 v169, 16, v105
	v_add_f32_e32 v162, v168, v169
	v_and_b32_e32 v168, 0xffff0000, v89
	v_and_b32_e32 v169, 0xffff0000, v105
	v_add_f32_e32 v163, v168, v169
	v_lshlrev_b32_e32 v168, 16, v90
	v_lshlrev_b32_e32 v169, 16, v106
	v_add_f32_e32 v164, v168, v169
	v_and_b32_e32 v168, 0xffff0000, v90
	v_and_b32_e32 v169, 0xffff0000, v106
	v_add_f32_e32 v165, v168, v169
	v_lshlrev_b32_e32 v168, 16, v91
	v_lshlrev_b32_e32 v169, 16, v107
	v_add_f32_e32 v166, v168, v169
	v_and_b32_e32 v168, 0xffff0000, v91
	v_and_b32_e32 v169, 0xffff0000, v107
	v_add_f32_e32 v167, v168, v169
	v_add_f32_e32 v170, v160, v161
	v_add_f32_e32 v170, v170, v162
	v_add_f32_e32 v170, v170, v163
	v_add_f32_e32 v170, v170, v164
	v_add_f32_e32 v170, v170, v165
	v_add_f32_e32 v170, v170, v166
	v_add_f32_e32 v170, v170, v167
	s_nop 1
	v_add_f32_dpp v170, v170, v170 quad_perm:[1,0,3,2] row_mask:0xf bank_mask:0xf bound_ctrl:1
	s_nop 1
	v_add_f32_dpp v170, v170, v170 quad_perm:[2,3,0,1] row_mask:0xf bank_mask:0xf bound_ctrl:1
	s_nop 1
	v_add_f32_dpp v170, v170, v170 row_half_mirror row_mask:0xf bank_mask:0xf bound_ctrl:1
	v_mul_f32_e32 v170, 0x3c800000, v170
	v_sub_f32_e32 v160, v160, v170
	v_sub_f32_e32 v161, v161, v170
	v_sub_f32_e32 v162, v162, v170
	v_sub_f32_e32 v163, v163, v170
	v_sub_f32_e32 v164, v164, v170
	v_sub_f32_e32 v165, v165, v170
	v_sub_f32_e32 v166, v166, v170
	v_sub_f32_e32 v167, v167, v170
	v_mul_f32_e32 v171, v160, v160
	v_fmac_f32_e32 v171, v161, v161
	v_fmac_f32_e32 v171, v162, v162
	v_fmac_f32_e32 v171, v163, v163
	v_fmac_f32_e32 v171, v164, v164
	v_fmac_f32_e32 v171, v165, v165
	v_fmac_f32_e32 v171, v166, v166
	v_fmac_f32_e32 v171, v167, v167
	s_nop 1
	v_add_f32_dpp v171, v171, v171 quad_perm:[1,0,3,2] row_mask:0xf bank_mask:0xf bound_ctrl:1
	s_nop 1
	v_add_f32_dpp v171, v171, v171 quad_perm:[2,3,0,1] row_mask:0xf bank_mask:0xf bound_ctrl:1
	s_nop 1
	v_add_f32_dpp v171, v171, v171 row_half_mirror row_mask:0xf bank_mask:0xf bound_ctrl:1
	v_mov_b32_e32 v172, 0x3a27c5ac
	v_fmac_f32_e32 v172, 0x3c800000, v171
	v_rsq_f32_e32 v172, v172
	v_add_f32_e32 v173, v146, v150
	s_nop 0
	v_mul_f32_e32 v160, v160, v172
	v_mul_f32_e32 v161, v161, v172
	v_mul_f32_e32 v162, v162, v172
	v_mul_f32_e32 v163, v163, v172
	v_mul_f32_e32 v164, v164, v172
	v_mul_f32_e32 v165, v165, v172
	v_mul_f32_e32 v166, v166, v172
	v_mul_f32_e32 v167, v167, v172
	v_fma_f32 v160, v26, v160, v58
	v_fma_f32 v161, v27, v161, v59
	v_fma_f32 v162, v28, v162, v60
	v_fma_f32 v163, v29, v163, v61
	v_fma_f32 v164, v30, v164, v62
	v_fma_f32 v165, v31, v165, v63
	v_fma_f32 v166, v32, v166, v64
	v_fma_f32 v167, v33, v167, v65
	v_lshlrev_b32_e32 v168, 16, v120
	v_fmac_f32_e32 v160, v173, v168
	v_and_b32_e32 v169, 0xffff0000, v120
	v_fmac_f32_e32 v161, v173, v169
	v_lshlrev_b32_e32 v168, 16, v136
	v_mul_f32_e32 v160, v160, v168
	v_and_b32_e32 v169, 0xffff0000, v136
	v_mul_f32_e32 v161, v161, v169
	v_lshlrev_b32_e32 v168, 16, v121
	v_fmac_f32_e32 v162, v173, v168
	v_and_b32_e32 v169, 0xffff0000, v121
	v_fmac_f32_e32 v163, v173, v169
	v_lshlrev_b32_e32 v168, 16, v137
	v_mul_f32_e32 v162, v162, v168
	v_and_b32_e32 v169, 0xffff0000, v137
	v_mul_f32_e32 v163, v163, v169
	v_lshlrev_b32_e32 v168, 16, v122
	v_fmac_f32_e32 v164, v173, v168
	v_and_b32_e32 v169, 0xffff0000, v122
	v_fmac_f32_e32 v165, v173, v169
	v_lshlrev_b32_e32 v168, 16, v138
	v_mul_f32_e32 v164, v164, v168
	v_and_b32_e32 v169, 0xffff0000, v138
	v_mul_f32_e32 v165, v165, v169
	v_lshlrev_b32_e32 v168, 16, v123
	v_fmac_f32_e32 v166, v173, v168
	v_and_b32_e32 v169, 0xffff0000, v123
	v_fmac_f32_e32 v167, v173, v169
	v_lshlrev_b32_e32 v168, 16, v139
	v_mul_f32_e32 v166, v166, v168
	v_and_b32_e32 v169, 0xffff0000, v139
	v_mul_f32_e32 v167, v167, v169
	v_cvt_pk_bf16_f32 v192, v160, v161
	v_cvt_pk_bf16_f32 v193, v162, v163
	v_cvt_pk_bf16_f32 v194, v164, v165
	v_cvt_pk_bf16_f32 v195, v166, v167
	global_store_dwordx4 v5, v[192:195], s[12:13] offset:2048
	v_lshlrev_b32_e32 v168, 16, v92
	v_lshlrev_b32_e32 v169, 16, v108
	v_add_f32_e32 v160, v168, v169
	v_and_b32_e32 v168, 0xffff0000, v92
	v_and_b32_e32 v169, 0xffff0000, v108
	v_add_f32_e32 v161, v168, v169
	v_lshlrev_b32_e32 v168, 16, v93
	v_lshlrev_b32_e32 v169, 16, v109
	v_add_f32_e32 v162, v168, v169
	v_and_b32_e32 v168, 0xffff0000, v93
	v_and_b32_e32 v169, 0xffff0000, v109
	v_add_f32_e32 v163, v168, v169
	v_lshlrev_b32_e32 v168, 16, v94
	v_lshlrev_b32_e32 v169, 16, v110
	v_add_f32_e32 v164, v168, v169
	v_and_b32_e32 v168, 0xffff0000, v94
	v_and_b32_e32 v169, 0xffff0000, v110
	v_add_f32_e32 v165, v168, v169
	v_lshlrev_b32_e32 v168, 16, v95
	v_lshlrev_b32_e32 v169, 16, v111
	v_add_f32_e32 v166, v168, v169
	v_and_b32_e32 v168, 0xffff0000, v95
	v_and_b32_e32 v169, 0xffff0000, v111
	v_add_f32_e32 v167, v168, v169
	v_add_f32_e32 v170, v160, v161
	v_add_f32_e32 v170, v170, v162
	v_add_f32_e32 v170, v170, v163
	v_add_f32_e32 v170, v170, v164
	v_add_f32_e32 v170, v170, v165
	v_add_f32_e32 v170, v170, v166
	v_add_f32_e32 v170, v170, v167
	s_nop 1
	v_add_f32_dpp v170, v170, v170 quad_perm:[1,0,3,2] row_mask:0xf bank_mask:0xf bound_ctrl:1
	s_nop 1
	v_add_f32_dpp v170, v170, v170 quad_perm:[2,3,0,1] row_mask:0xf bank_mask:0xf bound_ctrl:1
	s_nop 1
	v_add_f32_dpp v170, v170, v170 row_half_mirror row_mask:0xf bank_mask:0xf bound_ctrl:1
	v_mul_f32_e32 v170, 0x3c800000, v170
	v_sub_f32_e32 v160, v160, v170
	v_sub_f32_e32 v161, v161, v170
	v_sub_f32_e32 v162, v162, v170
	v_sub_f32_e32 v163, v163, v170
	v_sub_f32_e32 v164, v164, v170
	v_sub_f32_e32 v165, v165, v170
	v_sub_f32_e32 v166, v166, v170
	v_sub_f32_e32 v167, v167, v170
	v_mul_f32_e32 v171, v160, v160
	v_fmac_f32_e32 v171, v161, v161
	v_fmac_f32_e32 v171, v162, v162
	v_fmac_f32_e32 v171, v163, v163
	v_fmac_f32_e32 v171, v164, v164
	v_fmac_f32_e32 v171, v165, v165
	v_fmac_f32_e32 v171, v166, v166
	v_fmac_f32_e32 v171, v167, v167
	s_nop 1
	v_add_f32_dpp v171, v171, v171 quad_perm:[1,0,3,2] row_mask:0xf bank_mask:0xf bound_ctrl:1
	s_nop 1
	v_add_f32_dpp v171, v171, v171 quad_perm:[2,3,0,1] row_mask:0xf bank_mask:0xf bound_ctrl:1
	s_nop 1
	v_add_f32_dpp v171, v171, v171 row_half_mirror row_mask:0xf bank_mask:0xf bound_ctrl:1
	v_mov_b32_e32 v172, 0x3a27c5ac
	v_fmac_f32_e32 v172, 0x3c800000, v171
	v_rsq_f32_e32 v172, v172
	v_add_f32_e32 v173, v147, v151
	s_nop 0
	v_mul_f32_e32 v160, v160, v172
	v_mul_f32_e32 v161, v161, v172
	v_mul_f32_e32 v162, v162, v172
	v_mul_f32_e32 v163, v163, v172
	v_mul_f32_e32 v164, v164, v172
	v_mul_f32_e32 v165, v165, v172
	v_mul_f32_e32 v166, v166, v172
	v_mul_f32_e32 v167, v167, v172
	v_fma_f32 v160, v34, v160, v66
	v_fma_f32 v161, v35, v161, v67
	v_fma_f32 v162, v36, v162, v68
	v_fma_f32 v163, v37, v163, v69
	v_fma_f32 v164, v38, v164, v70
	v_fma_f32 v165, v39, v165, v71
	v_fma_f32 v166, v40, v166, v72
	v_fma_f32 v167, v41, v167, v73
	v_lshlrev_b32_e32 v168, 16, v124
	v_fmac_f32_e32 v160, v173, v168
	v_and_b32_e32 v169, 0xffff0000, v124
	v_fmac_f32_e32 v161, v173, v169
	v_lshlrev_b32_e32 v168, 16, v140
	v_mul_f32_e32 v160, v160, v168
	v_and_b32_e32 v169, 0xffff0000, v140
	v_mul_f32_e32 v161, v161, v169
	v_lshlrev_b32_e32 v168, 16, v125
	v_fmac_f32_e32 v162, v173, v168
	v_and_b32_e32 v169, 0xffff0000, v125
	v_fmac_f32_e32 v163, v173, v169
	v_lshlrev_b32_e32 v168, 16, v141
	v_mul_f32_e32 v162, v162, v168
	v_and_b32_e32 v169, 0xffff0000, v141
	v_mul_f32_e32 v163, v163, v169
	v_lshlrev_b32_e32 v168, 16, v126
	v_fmac_f32_e32 v164, v173, v168
	v_and_b32_e32 v169, 0xffff0000, v126
	v_fmac_f32_e32 v165, v173, v169
	v_lshlrev_b32_e32 v168, 16, v142
	v_mul_f32_e32 v164, v164, v168
	v_and_b32_e32 v169, 0xffff0000, v142
	v_mul_f32_e32 v165, v165, v169
	v_lshlrev_b32_e32 v168, 16, v127
	v_fmac_f32_e32 v166, v173, v168
	v_and_b32_e32 v169, 0xffff0000, v127
	v_fmac_f32_e32 v167, v173, v169
	v_lshlrev_b32_e32 v168, 16, v143
	v_mul_f32_e32 v166, v166, v168
	v_and_b32_e32 v169, 0xffff0000, v143
	v_mul_f32_e32 v167, v167, v169
	v_cvt_pk_bf16_f32 v196, v160, v161
	v_cvt_pk_bf16_f32 v197, v162, v163
	v_cvt_pk_bf16_f32 v198, v164, v165
	v_cvt_pk_bf16_f32 v199, v166, v167
	global_store_dwordx4 v5, v[196:199], s[12:13] offset:3072
	s_add_i32 s24, s24, 1
	s_cmp_lt_u32 s24, 32
	s_cbranch_scc1 .Lx14_row
	s_waitcnt vmcnt(0)
	s_cmp_lg_u32 s82, 0
	s_cbranch_scc1 .Lx14_fin_other
	s_mov_b32 s27, 0
	v_mov_b32_e32 v5, 0x200
